# P1 row loop with two rows of loads in flight per wave (loop unrolled by two over a second buffer), padded so that all later code keeps the previous placement mod 64
# speedup vs baseline: 1.0083x; 1.0024x over previous
.LBB0_103:
	v_lshl_add_u64 v[18:19], v[140:141], 0, s[18:19]
	v_add_co_u32_e32 v2, vcc, 0x2000, v18
	s_nop 1
	v_addc_co_u32_e32 v3, vcc, 0, v19, vcc
	v_add_co_u32_e32 v18, vcc, 0x3000, v18
	global_load_dwordx4 v[14:17], v[2:3], off nt
	global_load_dwordx4 v[10:13], v[2:3], off offset:1024 nt
	global_load_dwordx4 v[6:9], v[2:3], off offset:2048 nt
	s_nop 0
	global_load_dwordx4 v[2:5], v[2:3], off offset:3072 nt
	v_addc_co_u32_e32 v19, vcc, 0, v19, vcc
	global_load_dwordx4 v[30:33], v[18:19], off nt
	global_load_dwordx4 v[26:29], v[18:19], off offset:1024 nt
	global_load_dwordx4 v[22:25], v[18:19], off offset:2048 nt
	s_nop 0
	global_load_dwordx4 v[18:21], v[18:19], off offset:3072 nt
	v_lshl_add_u64 v[176:177], v[140:141], 0, s[18:19]
	v_add_co_u32_e32 v160, vcc, 0x4000, v176
	s_nop 1
	v_addc_co_u32_e32 v161, vcc, 0, v177, vcc
	v_add_co_u32_e32 v176, vcc, 0x5000, v176
	global_load_dwordx4 v[172:175], v[160:161], off nt
	global_load_dwordx4 v[168:171], v[160:161], off offset:1024 nt
	global_load_dwordx4 v[164:167], v[160:161], off offset:2048 nt
	s_nop 0
	global_load_dwordx4 v[160:163], v[160:161], off offset:3072 nt
	v_addc_co_u32_e32 v177, vcc, 0, v177, vcc
	global_load_dwordx4 v[188:191], v[176:177], off nt
	global_load_dwordx4 v[184:187], v[176:177], off offset:1024 nt
	global_load_dwordx4 v[180:183], v[176:177], off offset:2048 nt
	s_nop 0
	global_load_dwordx4 v[176:179], v[176:177], off offset:3072 nt
	s_waitcnt vmcnt(16)
	s_branch .Lp1_head

.Lp1_head:
	v_mul_f32_e32 v154, v127, v127
	v_mul_f32_e32 v155, v123, v123
	v_fmac_f32_e32 v154, v126, v126
	v_fmac_f32_e32 v155, v122, v122
	v_fmac_f32_e32 v154, v128, v128
	v_fmac_f32_e32 v155, v124, v124
	v_fmac_f32_e32 v154, v129, v129
	v_fmac_f32_e32 v155, v125, v125
	v_add_f32_e32 v154, v154, v155
	v_mul_f32_e32 v155, v119, v119
	v_fmac_f32_e32 v155, v118, v118
	v_fmac_f32_e32 v155, v120, v120
	v_fmac_f32_e32 v155, v121, v121
	v_add_f32_e32 v154, v155, v154
	v_mul_f32_e32 v155, v115, v115
	v_fmac_f32_e32 v155, v114, v114
	v_fmac_f32_e32 v155, v116, v116
	v_fmac_f32_e32 v155, v117, v117
	v_add_f32_e32 v154, v155, v154
	v_mul_f32_e32 v155, v111, v111
	v_fmac_f32_e32 v155, v110, v110
	v_fmac_f32_e32 v155, v112, v112
	v_fmac_f32_e32 v155, v113, v113
	v_add_f32_e32 v154, v155, v154
	v_mul_f32_e32 v155, v107, v107
	v_fmac_f32_e32 v155, v106, v106
	v_fmac_f32_e32 v155, v108, v108
	v_fmac_f32_e32 v155, v109, v109
	v_add_f32_e32 v154, v155, v154
	v_mul_f32_e32 v155, v103, v103
	v_fmac_f32_e32 v155, v102, v102
	v_fmac_f32_e32 v155, v104, v104
	v_fmac_f32_e32 v155, v105, v105
	v_add_f32_e32 v154, v155, v154
	v_mul_f32_e32 v155, v83, v83
	v_fmac_f32_e32 v155, v82, v82
	v_fmac_f32_e32 v155, v84, v84
	v_fmac_f32_e32 v155, v85, v85
	v_add_f32_e32 v154, v155, v154
	v_mov_b32_e32 v157, 0
	s_add_u32 s18, s18, 0x2000
	v_add_f32_dpp v154, v154, v154 quad_perm:[1,0,3,2] row_mask:0xf bank_mask:0xf bound_ctrl:1
	s_addc_u32 s19, s19, 0
	s_cmp_eq_u32 s18, 0x20000
	v_add_f32_dpp v154, v154, v154 quad_perm:[2,3,0,1] row_mask:0xf bank_mask:0xf bound_ctrl:1
	s_nop 1
	v_add_f32_dpp v154, v154, v154 row_half_mirror row_mask:0xf bank_mask:0xf bound_ctrl:1
	s_nop 1
	v_add_f32_dpp v154, v154, v154 row_mirror row_mask:0xf bank_mask:0xf bound_ctrl:1
	v_mov_b32_e32 v155, v154
	s_nop 1
	v_permlane16_swap_b32_e32 v154, v155
	v_add_f32_e32 v154, v154, v155
	v_mov_b32_e32 v155, v154
	s_nop 1
	v_permlane32_swap_b32_e32 v154, v155
	v_add_f32_e32 v154, v154, v155
	v_fmamk_f32 v154, v154, 0x3a000000, v152
	v_mul_f32_e32 v155, 0x4b800000, v154
	v_cmp_gt_f32_e32 vcc, s21, v154
	s_nop 1
	v_cndmask_b32_e32 v154, v154, v155, vcc
	v_rsq_f32_e32 v154, v154
	s_nop 0
	v_mul_f32_e32 v155, 0x45800000, v154
	v_cndmask_b32_e32 v154, v154, v155, vcc
	v_pk_mul_f32 v[126:127], v[126:127], v[154:155] op_sel_hi:[1,0]
	v_pk_mul_f32 v[128:129], v[128:129], v[154:155] op_sel_hi:[1,0]
	s_waitcnt lgkmcnt(13)
	v_pk_fma_f32 v[126:127], v[34:35], v[126:127], v[42:43]
	v_pk_fma_f32 v[128:129], v[36:37], v[128:129], v[44:45]
	v_med3_f32 v155, v126, s22, v153
	v_med3_f32 v156, v127, s22, v153
	v_cvt_pk_fp8_f32 v157, v155, v156
	v_med3_f32 v155, v128, s22, v153
	v_med3_f32 v156, v129, s22, v153
	v_pk_mul_f32 v[122:123], v[122:123], v[154:155] op_sel_hi:[1,0]
	v_cvt_pk_fp8_f32 v157, v155, v156 op_sel:[0,0,1]
	v_cvt_pk_bf16_f32 v126, v126, v127
	v_cvt_pk_bf16_f32 v127, v128, v129
	s_waitcnt lgkmcnt(12)
	v_pk_fma_f32 v[122:123], v[122:123], v[38:39], v[46:47]
	global_store_dwordx2 v[146:147], v[126:127], off offset:-2048
	global_store_dword v[148:149], v157, off offset:-1024
	v_med3_f32 v126, v122, s22, v153
	v_med3_f32 v127, v123, s22, v153
	v_mov_b32_e32 v128, 0
	v_cvt_pk_fp8_f32 v128, v126, v127
	v_pk_mul_f32 v[124:125], v[124:125], v[154:155] op_sel_hi:[1,0]
	v_pk_mul_f32 v[118:119], v[118:119], v[154:155] op_sel_hi:[1,0]
	v_pk_fma_f32 v[124:125], v[124:125], v[40:41], v[48:49]
	v_cvt_pk_bf16_f32 v122, v122, v123
	v_med3_f32 v126, v124, s22, v153
	v_med3_f32 v127, v125, s22, v153
	v_cvt_pk_fp8_f32 v128, v126, v127 op_sel:[0,0,1]
	v_cvt_pk_bf16_f32 v123, v124, v125
	s_waitcnt lgkmcnt(9)
	v_pk_fma_f32 v[118:119], v[118:119], v[50:51], v[58:59]
	global_store_dwordx2 v[146:147], v[122:123], off offset:-1536
	global_store_dword v[148:149], v128, off offset:-768
	v_med3_f32 v122, v118, s22, v153
	v_med3_f32 v123, v119, s22, v153
	v_mov_b32_e32 v124, 0
	v_cvt_pk_fp8_f32 v124, v122, v123
	v_pk_mul_f32 v[120:121], v[120:121], v[154:155] op_sel_hi:[1,0]
	v_pk_mul_f32 v[114:115], v[114:115], v[154:155] op_sel_hi:[1,0]
	v_pk_fma_f32 v[120:121], v[120:121], v[52:53], v[60:61]
	v_cvt_pk_bf16_f32 v118, v118, v119
	v_med3_f32 v122, v120, s22, v153
	v_med3_f32 v123, v121, s22, v153
	v_cvt_pk_fp8_f32 v124, v122, v123 op_sel:[0,0,1]
	v_cvt_pk_bf16_f32 v119, v120, v121
	s_waitcnt lgkmcnt(8)
	v_pk_fma_f32 v[114:115], v[114:115], v[54:55], v[62:63]
	global_store_dwordx2 v[146:147], v[118:119], off offset:-1024
	global_store_dword v[148:149], v124, off offset:-512
	v_med3_f32 v118, v114, s22, v153
	v_med3_f32 v119, v115, s22, v153
	v_mov_b32_e32 v120, 0
	v_cvt_pk_fp8_f32 v120, v118, v119
	v_pk_mul_f32 v[116:117], v[116:117], v[154:155] op_sel_hi:[1,0]
	v_pk_mul_f32 v[110:111], v[110:111], v[154:155] op_sel_hi:[1,0]
	v_pk_fma_f32 v[116:117], v[116:117], v[56:57], v[64:65]
	v_cvt_pk_bf16_f32 v114, v114, v115
	v_med3_f32 v118, v116, s22, v153
	v_med3_f32 v119, v117, s22, v153
	v_cvt_pk_fp8_f32 v120, v118, v119 op_sel:[0,0,1]
	v_cvt_pk_bf16_f32 v115, v116, v117
	s_waitcnt lgkmcnt(5)
	v_pk_fma_f32 v[110:111], v[110:111], v[66:67], v[74:75]
	global_store_dwordx2 v[146:147], v[114:115], off offset:-512
	global_store_dword v[148:149], v120, off offset:-256
	v_med3_f32 v114, v110, s22, v153
	v_med3_f32 v115, v111, s22, v153
	v_mov_b32_e32 v116, 0
	v_cvt_pk_fp8_f32 v116, v114, v115
	v_pk_mul_f32 v[112:113], v[112:113], v[154:155] op_sel_hi:[1,0]
	v_pk_mul_f32 v[106:107], v[106:107], v[154:155] op_sel_hi:[1,0]
	v_pk_fma_f32 v[112:113], v[112:113], v[68:69], v[76:77]
	v_cvt_pk_bf16_f32 v110, v110, v111
	v_med3_f32 v114, v112, s22, v153
	v_med3_f32 v115, v113, s22, v153
	v_cvt_pk_fp8_f32 v116, v114, v115 op_sel:[0,0,1]
	v_cvt_pk_bf16_f32 v111, v112, v113
	s_waitcnt lgkmcnt(4)
	v_pk_fma_f32 v[106:107], v[106:107], v[70:71], v[78:79]
	global_store_dwordx2 v[146:147], v[110:111], off
	global_store_dword v[148:149], v116, off
	v_med3_f32 v110, v106, s22, v153
	v_med3_f32 v111, v107, s22, v153
	v_mov_b32_e32 v112, 0
	v_cvt_pk_fp8_f32 v112, v110, v111
	v_pk_mul_f32 v[108:109], v[108:109], v[154:155] op_sel_hi:[1,0]
	v_pk_mul_f32 v[102:103], v[102:103], v[154:155] op_sel_hi:[1,0]
	v_pk_fma_f32 v[108:109], v[108:109], v[72:73], v[80:81]
	v_cvt_pk_bf16_f32 v106, v106, v107
	v_med3_f32 v110, v108, s22, v153
	v_med3_f32 v111, v109, s22, v153
	v_cvt_pk_fp8_f32 v112, v110, v111 op_sel:[0,0,1]
	v_cvt_pk_bf16_f32 v107, v108, v109
	s_waitcnt lgkmcnt(1)
	v_pk_fma_f32 v[102:103], v[102:103], v[86:87], v[94:95]
	global_store_dwordx2 v[146:147], v[106:107], off offset:512
	global_store_dword v[148:149], v112, off offset:256
	v_med3_f32 v106, v102, s22, v153
	v_med3_f32 v107, v103, s22, v153
	v_mov_b32_e32 v108, 0
	v_cvt_pk_fp8_f32 v108, v106, v107
	v_pk_mul_f32 v[104:105], v[104:105], v[154:155] op_sel_hi:[1,0]
	v_pk_mul_f32 v[82:83], v[82:83], v[154:155] op_sel_hi:[1,0]
	v_pk_fma_f32 v[104:105], v[104:105], v[88:89], v[96:97]
	v_cvt_pk_bf16_f32 v102, v102, v103
	v_med3_f32 v106, v104, s22, v153
	v_med3_f32 v107, v105, s22, v153
	v_cvt_pk_fp8_f32 v108, v106, v107 op_sel:[0,0,1]
	v_cvt_pk_bf16_f32 v103, v104, v105
	s_waitcnt lgkmcnt(0)
	v_pk_fma_f32 v[82:83], v[82:83], v[90:91], v[98:99]
	global_store_dwordx2 v[146:147], v[102:103], off offset:1024
	global_store_dword v[148:149], v108, off offset:512
	v_med3_f32 v102, v82, s22, v153
	v_med3_f32 v103, v83, s22, v153
	v_mov_b32_e32 v104, 0
	v_cvt_pk_fp8_f32 v104, v102, v103
	v_pk_mul_f32 v[84:85], v[84:85], v[154:155] op_sel_hi:[1,0]
	v_cvt_pk_bf16_f32 v82, v82, v83
	v_pk_fma_f32 v[84:85], v[84:85], v[92:93], v[100:101]
	s_nop 0
	v_med3_f32 v102, v84, s22, v153
	v_med3_f32 v103, v85, s22, v153
	v_cvt_pk_fp8_f32 v104, v102, v103 op_sel:[0,0,1]
	v_cvt_pk_bf16_f32 v83, v84, v85
	global_store_dwordx2 v[146:147], v[82:83], off offset:1536
	global_store_dword v[148:149], v104, off offset:768
	v_lshl_add_u64 v[148:149], v[148:149], 0, s[12:13]
	v_lshl_add_u64 v[146:147], v[146:147], 0, s[14:15]
	s_cbranch_scc1 .LBB0_99
	s_waitcnt vmcnt(24)
	v_mov_b32_e32 v126, v14
	v_mov_b32_e32 v127, v15
	v_mov_b32_e32 v128, v16
	v_mov_b32_e32 v129, v17
	v_mov_b32_e32 v122, v10
	v_mov_b32_e32 v123, v11
	v_mov_b32_e32 v124, v12
	v_mov_b32_e32 v125, v13
	v_mov_b32_e32 v118, v6
	v_mov_b32_e32 v119, v7
	v_mov_b32_e32 v120, v8
	v_mov_b32_e32 v121, v9
	v_mov_b32_e32 v114, v2
	v_mov_b32_e32 v115, v3
	v_mov_b32_e32 v116, v4
	v_mov_b32_e32 v117, v5
	v_mov_b32_e32 v110, v30
	v_mov_b32_e32 v111, v31
	v_mov_b32_e32 v112, v32
	v_mov_b32_e32 v113, v33
	v_mov_b32_e32 v106, v26
	v_mov_b32_e32 v107, v27
	v_mov_b32_e32 v108, v28
	v_mov_b32_e32 v109, v29
	v_mov_b32_e32 v102, v22
	v_mov_b32_e32 v103, v23
	v_mov_b32_e32 v104, v24
	v_mov_b32_e32 v105, v25
	v_mov_b32_e32 v82, v18
	v_mov_b32_e32 v83, v19
	v_mov_b32_e32 v84, v20
	v_mov_b32_e32 v85, v21
	s_cmp_gt_u32 s18, 0x1a000
	s_cbranch_scc1 .Lp1_head2
	v_lshl_add_u64 v[18:19], v[140:141], 0, s[18:19]
	v_add_co_u32_e32 v2, vcc, 0x4000, v18
	s_nop 1
	v_addc_co_u32_e32 v3, vcc, 0, v19, vcc
	v_add_co_u32_e32 v18, vcc, 0x5000, v18
	global_load_dwordx4 v[14:17], v[2:3], off nt
	global_load_dwordx4 v[10:13], v[2:3], off offset:1024 nt
	global_load_dwordx4 v[6:9], v[2:3], off offset:2048 nt
	s_nop 0
	global_load_dwordx4 v[2:5], v[2:3], off offset:3072 nt
	v_addc_co_u32_e32 v19, vcc, 0, v19, vcc
	global_load_dwordx4 v[30:33], v[18:19], off nt
	global_load_dwordx4 v[26:29], v[18:19], off offset:1024 nt
	global_load_dwordx4 v[22:25], v[18:19], off offset:2048 nt
	s_nop 0
	global_load_dwordx4 v[18:21], v[18:19], off offset:3072 nt
.Lp1_head2:
	v_mul_f32_e32 v154, v127, v127
	v_mul_f32_e32 v155, v123, v123
	v_fmac_f32_e32 v154, v126, v126
	v_fmac_f32_e32 v155, v122, v122
	v_fmac_f32_e32 v154, v128, v128
	v_fmac_f32_e32 v155, v124, v124
	v_fmac_f32_e32 v154, v129, v129
	v_fmac_f32_e32 v155, v125, v125
	v_add_f32_e32 v154, v154, v155
	v_mul_f32_e32 v155, v119, v119
	v_fmac_f32_e32 v155, v118, v118
	v_fmac_f32_e32 v155, v120, v120
	v_fmac_f32_e32 v155, v121, v121
	v_add_f32_e32 v154, v155, v154
	v_mul_f32_e32 v155, v115, v115
	v_fmac_f32_e32 v155, v114, v114
	v_fmac_f32_e32 v155, v116, v116
	v_fmac_f32_e32 v155, v117, v117
	v_add_f32_e32 v154, v155, v154
	v_mul_f32_e32 v155, v111, v111
	v_fmac_f32_e32 v155, v110, v110
	v_fmac_f32_e32 v155, v112, v112
	v_fmac_f32_e32 v155, v113, v113
	v_add_f32_e32 v154, v155, v154
	v_mul_f32_e32 v155, v107, v107
	v_fmac_f32_e32 v155, v106, v106
	v_fmac_f32_e32 v155, v108, v108
	v_fmac_f32_e32 v155, v109, v109
	v_add_f32_e32 v154, v155, v154
	v_mul_f32_e32 v155, v103, v103
	v_fmac_f32_e32 v155, v102, v102
	v_fmac_f32_e32 v155, v104, v104
	v_fmac_f32_e32 v155, v105, v105
	v_add_f32_e32 v154, v155, v154
	v_mul_f32_e32 v155, v83, v83
	v_fmac_f32_e32 v155, v82, v82
	v_fmac_f32_e32 v155, v84, v84
	v_fmac_f32_e32 v155, v85, v85
	v_add_f32_e32 v154, v155, v154
	v_mov_b32_e32 v157, 0
	s_add_u32 s18, s18, 0x2000
	v_add_f32_dpp v154, v154, v154 quad_perm:[1,0,3,2] row_mask:0xf bank_mask:0xf bound_ctrl:1
	s_addc_u32 s19, s19, 0
	s_cmp_eq_u32 s18, 0x20000
	v_add_f32_dpp v154, v154, v154 quad_perm:[2,3,0,1] row_mask:0xf bank_mask:0xf bound_ctrl:1
	s_nop 1
	v_add_f32_dpp v154, v154, v154 row_half_mirror row_mask:0xf bank_mask:0xf bound_ctrl:1
	s_nop 1
	v_add_f32_dpp v154, v154, v154 row_mirror row_mask:0xf bank_mask:0xf bound_ctrl:1
	v_mov_b32_e32 v155, v154
	s_nop 1
	v_permlane16_swap_b32_e32 v154, v155
	v_add_f32_e32 v154, v154, v155
	v_mov_b32_e32 v155, v154
	s_nop 1
	v_permlane32_swap_b32_e32 v154, v155
	v_add_f32_e32 v154, v154, v155
	v_fmamk_f32 v154, v154, 0x3a000000, v152
	v_mul_f32_e32 v155, 0x4b800000, v154
	v_cmp_gt_f32_e32 vcc, s21, v154
	s_nop 1
	v_cndmask_b32_e32 v154, v154, v155, vcc
	v_rsq_f32_e32 v154, v154
	s_nop 0
	v_mul_f32_e32 v155, 0x45800000, v154
	v_cndmask_b32_e32 v154, v154, v155, vcc
	v_pk_mul_f32 v[126:127], v[126:127], v[154:155] op_sel_hi:[1,0]
	v_pk_mul_f32 v[128:129], v[128:129], v[154:155] op_sel_hi:[1,0]
	s_waitcnt lgkmcnt(13)
	v_pk_fma_f32 v[126:127], v[34:35], v[126:127], v[42:43]
	v_pk_fma_f32 v[128:129], v[36:37], v[128:129], v[44:45]
	v_med3_f32 v155, v126, s22, v153
	v_med3_f32 v156, v127, s22, v153
	v_cvt_pk_fp8_f32 v157, v155, v156
	v_med3_f32 v155, v128, s22, v153
	v_med3_f32 v156, v129, s22, v153
	v_pk_mul_f32 v[122:123], v[122:123], v[154:155] op_sel_hi:[1,0]
	v_cvt_pk_fp8_f32 v157, v155, v156 op_sel:[0,0,1]
	v_cvt_pk_bf16_f32 v126, v126, v127
	v_cvt_pk_bf16_f32 v127, v128, v129
	s_waitcnt lgkmcnt(12)
	v_pk_fma_f32 v[122:123], v[122:123], v[38:39], v[46:47]
	global_store_dwordx2 v[146:147], v[126:127], off offset:-2048
	global_store_dword v[148:149], v157, off offset:-1024
	v_med3_f32 v126, v122, s22, v153
	v_med3_f32 v127, v123, s22, v153
	v_mov_b32_e32 v128, 0
	v_cvt_pk_fp8_f32 v128, v126, v127
	v_pk_mul_f32 v[124:125], v[124:125], v[154:155] op_sel_hi:[1,0]
	v_pk_mul_f32 v[118:119], v[118:119], v[154:155] op_sel_hi:[1,0]
	v_pk_fma_f32 v[124:125], v[124:125], v[40:41], v[48:49]
	v_cvt_pk_bf16_f32 v122, v122, v123
	v_med3_f32 v126, v124, s22, v153
	v_med3_f32 v127, v125, s22, v153
	v_cvt_pk_fp8_f32 v128, v126, v127 op_sel:[0,0,1]
	v_cvt_pk_bf16_f32 v123, v124, v125
	s_waitcnt lgkmcnt(9)
	v_pk_fma_f32 v[118:119], v[118:119], v[50:51], v[58:59]
	global_store_dwordx2 v[146:147], v[122:123], off offset:-1536
	global_store_dword v[148:149], v128, off offset:-768
	v_med3_f32 v122, v118, s22, v153
	v_med3_f32 v123, v119, s22, v153
	v_mov_b32_e32 v124, 0
	v_cvt_pk_fp8_f32 v124, v122, v123
	v_pk_mul_f32 v[120:121], v[120:121], v[154:155] op_sel_hi:[1,0]
	v_pk_mul_f32 v[114:115], v[114:115], v[154:155] op_sel_hi:[1,0]
	v_pk_fma_f32 v[120:121], v[120:121], v[52:53], v[60:61]
	v_cvt_pk_bf16_f32 v118, v118, v119
	v_med3_f32 v122, v120, s22, v153
	v_med3_f32 v123, v121, s22, v153
	v_cvt_pk_fp8_f32 v124, v122, v123 op_sel:[0,0,1]
	v_cvt_pk_bf16_f32 v119, v120, v121
	s_waitcnt lgkmcnt(8)
	v_pk_fma_f32 v[114:115], v[114:115], v[54:55], v[62:63]
	global_store_dwordx2 v[146:147], v[118:119], off offset:-1024
	global_store_dword v[148:149], v124, off offset:-512
	v_med3_f32 v118, v114, s22, v153
	v_med3_f32 v119, v115, s22, v153
	v_mov_b32_e32 v120, 0
	v_cvt_pk_fp8_f32 v120, v118, v119
	v_pk_mul_f32 v[116:117], v[116:117], v[154:155] op_sel_hi:[1,0]
	v_pk_mul_f32 v[110:111], v[110:111], v[154:155] op_sel_hi:[1,0]
	v_pk_fma_f32 v[116:117], v[116:117], v[56:57], v[64:65]
	v_cvt_pk_bf16_f32 v114, v114, v115
	v_med3_f32 v118, v116, s22, v153
	v_med3_f32 v119, v117, s22, v153
	v_cvt_pk_fp8_f32 v120, v118, v119 op_sel:[0,0,1]
	v_cvt_pk_bf16_f32 v115, v116, v117
	s_waitcnt lgkmcnt(5)
	v_pk_fma_f32 v[110:111], v[110:111], v[66:67], v[74:75]
	global_store_dwordx2 v[146:147], v[114:115], off offset:-512
	global_store_dword v[148:149], v120, off offset:-256
	v_med3_f32 v114, v110, s22, v153
	v_med3_f32 v115, v111, s22, v153
	v_mov_b32_e32 v116, 0
	v_cvt_pk_fp8_f32 v116, v114, v115
	v_pk_mul_f32 v[112:113], v[112:113], v[154:155] op_sel_hi:[1,0]
	v_pk_mul_f32 v[106:107], v[106:107], v[154:155] op_sel_hi:[1,0]
	v_pk_fma_f32 v[112:113], v[112:113], v[68:69], v[76:77]
	v_cvt_pk_bf16_f32 v110, v110, v111
	v_med3_f32 v114, v112, s22, v153
	v_med3_f32 v115, v113, s22, v153
	v_cvt_pk_fp8_f32 v116, v114, v115 op_sel:[0,0,1]
	v_cvt_pk_bf16_f32 v111, v112, v113
	s_waitcnt lgkmcnt(4)
	v_pk_fma_f32 v[106:107], v[106:107], v[70:71], v[78:79]
	global_store_dwordx2 v[146:147], v[110:111], off
	global_store_dword v[148:149], v116, off
	v_med3_f32 v110, v106, s22, v153
	v_med3_f32 v111, v107, s22, v153
	v_mov_b32_e32 v112, 0
	v_cvt_pk_fp8_f32 v112, v110, v111
	v_pk_mul_f32 v[108:109], v[108:109], v[154:155] op_sel_hi:[1,0]
	v_pk_mul_f32 v[102:103], v[102:103], v[154:155] op_sel_hi:[1,0]
	v_pk_fma_f32 v[108:109], v[108:109], v[72:73], v[80:81]
	v_cvt_pk_bf16_f32 v106, v106, v107
	v_med3_f32 v110, v108, s22, v153
	v_med3_f32 v111, v109, s22, v153
	v_cvt_pk_fp8_f32 v112, v110, v111 op_sel:[0,0,1]
	v_cvt_pk_bf16_f32 v107, v108, v109
	s_waitcnt lgkmcnt(1)
	v_pk_fma_f32 v[102:103], v[102:103], v[86:87], v[94:95]
	global_store_dwordx2 v[146:147], v[106:107], off offset:512
	global_store_dword v[148:149], v112, off offset:256
	v_med3_f32 v106, v102, s22, v153
	v_med3_f32 v107, v103, s22, v153
	v_mov_b32_e32 v108, 0
	v_cvt_pk_fp8_f32 v108, v106, v107
	v_pk_mul_f32 v[104:105], v[104:105], v[154:155] op_sel_hi:[1,0]
	v_pk_mul_f32 v[82:83], v[82:83], v[154:155] op_sel_hi:[1,0]
	v_pk_fma_f32 v[104:105], v[104:105], v[88:89], v[96:97]
	v_cvt_pk_bf16_f32 v102, v102, v103
	v_med3_f32 v106, v104, s22, v153
	v_med3_f32 v107, v105, s22, v153
	v_cvt_pk_fp8_f32 v108, v106, v107 op_sel:[0,0,1]
	v_cvt_pk_bf16_f32 v103, v104, v105
	s_waitcnt lgkmcnt(0)
	v_pk_fma_f32 v[82:83], v[82:83], v[90:91], v[98:99]
	global_store_dwordx2 v[146:147], v[102:103], off offset:1024
	global_store_dword v[148:149], v108, off offset:512
	v_med3_f32 v102, v82, s22, v153
	v_med3_f32 v103, v83, s22, v153
	v_mov_b32_e32 v104, 0
	v_cvt_pk_fp8_f32 v104, v102, v103
	v_pk_mul_f32 v[84:85], v[84:85], v[154:155] op_sel_hi:[1,0]
	v_cvt_pk_bf16_f32 v82, v82, v83
	v_pk_fma_f32 v[84:85], v[84:85], v[92:93], v[100:101]
	s_nop 0
	v_med3_f32 v102, v84, s22, v153
	v_med3_f32 v103, v85, s22, v153
	v_cvt_pk_fp8_f32 v104, v102, v103 op_sel:[0,0,1]
	v_cvt_pk_bf16_f32 v83, v84, v85
	global_store_dwordx2 v[146:147], v[82:83], off offset:1536
	global_store_dword v[148:149], v104, off offset:768
	v_lshl_add_u64 v[148:149], v[148:149], 0, s[12:13]
	v_lshl_add_u64 v[146:147], v[146:147], 0, s[14:15]
	s_cbranch_scc1 .LBB0_99
	s_waitcnt vmcnt(24)
	v_mov_b32_e32 v126, v172
	v_mov_b32_e32 v127, v173
	v_mov_b32_e32 v128, v174
	v_mov_b32_e32 v129, v175
	v_mov_b32_e32 v122, v168
	v_mov_b32_e32 v123, v169
	v_mov_b32_e32 v124, v170
	v_mov_b32_e32 v125, v171
	v_mov_b32_e32 v118, v164
	v_mov_b32_e32 v119, v165
	v_mov_b32_e32 v120, v166
	v_mov_b32_e32 v121, v167
	v_mov_b32_e32 v114, v160
	v_mov_b32_e32 v115, v161
	v_mov_b32_e32 v116, v162
	v_mov_b32_e32 v117, v163
	v_mov_b32_e32 v110, v188
	v_mov_b32_e32 v111, v189
	v_mov_b32_e32 v112, v190
	v_mov_b32_e32 v113, v191
	v_mov_b32_e32 v106, v184
	v_mov_b32_e32 v107, v185
	v_mov_b32_e32 v108, v186
	v_mov_b32_e32 v109, v187
	v_mov_b32_e32 v102, v180
	v_mov_b32_e32 v103, v181
	v_mov_b32_e32 v104, v182
	v_mov_b32_e32 v105, v183
	v_mov_b32_e32 v82, v176
	v_mov_b32_e32 v83, v177
	v_mov_b32_e32 v84, v178
	v_mov_b32_e32 v85, v179
	s_cmp_gt_u32 s18, 0x1a000
	s_cbranch_scc1 .Lp1_head
	v_lshl_add_u64 v[176:177], v[140:141], 0, s[18:19]
	v_add_co_u32_e32 v160, vcc, 0x4000, v176
	s_nop 1
	v_addc_co_u32_e32 v161, vcc, 0, v177, vcc
	v_add_co_u32_e32 v176, vcc, 0x5000, v176
	global_load_dwordx4 v[172:175], v[160:161], off nt
	global_load_dwordx4 v[168:171], v[160:161], off offset:1024 nt
	global_load_dwordx4 v[164:167], v[160:161], off offset:2048 nt
	s_nop 0
	global_load_dwordx4 v[160:163], v[160:161], off offset:3072 nt
	v_addc_co_u32_e32 v177, vcc, 0, v177, vcc
	global_load_dwordx4 v[188:191], v[176:177], off nt
	global_load_dwordx4 v[184:187], v[176:177], off offset:1024 nt
	global_load_dwordx4 v[180:183], v[176:177], off offset:2048 nt
	s_nop 0
	global_load_dwordx4 v[176:179], v[176:177], off offset:3072 nt
	s_branch .Lp1_head
	s_nop 0
	s_nop 0
	s_nop 0
	s_nop 0
	s_nop 0
	s_nop 0
	s_nop 0
